# conversion loops read the expert-weight base pointers once per phase instead of once per tile
# speedup vs baseline: 1.0091x; 1.0021x over previous
; #define LAS __attribute__((address_space(3)))
; __device__ __forceinline__ void conv8_queue(const Ctx& X, int n) {
;     LAS int* qw = (LAS int*)(X.lds + LDS_MISC + 64);
;     unsigned zo = 0; asm volatile("" : "+v"(zo));
;     int nb_ = 0;
;     if (X.tid == 0) nb_ = (int)__hip_atomic_fetch_add(XP_ctl(X) + CW_WQ + zo, (unsigned)(8 * CQ_CHUNK), __ATOMIC_RELAXED, __HIP_MEMORY_SCOPE_AGENT);
.LBB0_122:
	s_load_dwordx2 s[98:99], s[0:1], 0x70
	s_load_dwordx2 s[100:101], s[0:1], 0x80
	v_mov_b32_e32 v67, 0
	v_mov_b32_e32 v66, 0
	v_cmp_eq_u32_e64 s[2:3], 0, v0
	s_waitcnt vmcnt(0)
	v_lshl_add_u64 v[2:3], v[66:67], 2, s[90:91]
	v_mov_b32_e32 v76, 0
	s_and_saveexec_b64 s[8:9], s[2:3]
	s_cbranch_execz .LBB0_124
	v_add_co_u32_e32 v4, vcc, 0x14000, v2
	v_mov_b32_e32 v6, 16
	s_nop 0
	v_addc_co_u32_e32 v5, vcc, 0, v3, vcc
	global_atomic_add v76, v[4:5], v6, off sc0

; __device__ __forceinline__ Cvb conv8b_dec(const Ctx& X, int bit) { Cvb c; int kb, nb;
;     if (bit < I_GU8 / 8) { const int e = bit >> 8, r = bit & 255; kb = r >> 4; nb = r & 15; c.N = 2 * DFF; c.W = XP_w_gu(X) + (size_t)e * D * (2 * DFF); c.WT = XP_WguT(X) + (size_t)e * 16 * PAN_GU + (size_t)kb * PAN_GU; }
;     else { const int b2 = bit - I_GU8 / 8, e = b2 >> 7, r = b2 & 127; kb = r >> 3; nb = r & 7; c.N = D; c.W = XP_w_d(X) + (size_t)e * DFF * D; c.WT = XP_WdT(X) + (size_t)e * 16 * PAN_D + (size_t)kb * PAN_D; }
;     c.W += (size_t)(kb * 128 + 16 * X.wave) * c.N + nb * 256 + 4 * X.lane;
;     c.WT += (size_t)(nb * 256 + 32 * X.wave + (X.lane >> 3)) * 128 + 16 * (X.lane & 7);
; __device__ __forceinline__ void conv8_queue(const Ctx& X, int n) {
;     ...
;         const int base = __builtin_amdgcn_readfirstlane(*qw);
;         if (base >= n) break;
;         if (X.tid == 0) nb_ = (int)__hip_atomic_fetch_add(XP_ctl(X) + CW_WQ + zo, (unsigned)(8 * CQ_CHUNK), __ATOMIC_RELAXED, __HIP_MEMORY_SCOPE_AGENT);
;         const int left = (n - base) >> 3;
;         conv8b_run(X, base >> 3, 1, left < CQ_CHUNK ? left : CQ_CHUNK);
.LBB0_133:
	s_or_b64 exec, exec, s[8:9]
	s_sub_i32 s6, s14, s24
	s_ashr_i32 s23, s6, 3
	s_cmp_lt_i32 s23, 1
	s_cbranch_scc1 .LBB0_126
	s_ashr_i32 s22, s24, 3
	s_cmpk_gt_i32 s22, 0x1fff
	s_mov_b64 s[10:11], -1
	s_cbranch_scc0 .LBB0_136
	s_mov_b64 s[8:9], s[100:101]
	s_add_i32 s6, s22, 0xffffe000
	s_lshr_b32 s6, s6, 7
	s_bfe_u32 s25, s22, 0x40003
	s_bfe_u32 s26, s24, 0x30003
	s_lshl_b64 s[10:11], s[6:7], 24
	s_waitcnt lgkmcnt(0)
	s_add_u32 s8, s8, s10
	s_addc_u32 s9, s9, s11
	s_lshl_b64 s[10:11], s[6:7], 22
	s_add_u32 s12, s15, s10
	s_addc_u32 s13, s16, s11
	s_lshl_b32 s6, s25, 18
	s_mov_b64 s[10:11], 0
.LBB0_136:
	s_andn2_b64 vcc, exec, s[10:11]
	s_mov_b64 s[10:11], 0x800
	s_cbranch_vccnz .LBB0_138
	s_mov_b64 s[8:9], s[98:99]
	s_ashr_i32 s10, s24, 11
	s_ashr_i32 s11, s10, 31
	s_bfe_u32 s25, s22, 0x40004
	s_bfe_u32 s26, s24, 0x40003
	s_lshl_b64 s[12:13], s[10:11], 25
	s_waitcnt lgkmcnt(0)
	s_add_u32 s8, s8, s12
	s_addc_u32 s9, s9, s13
	s_lshl_b64 s[10:11], s[10:11], 23
	s_add_u32 s12, s17, s10
	s_addc_u32 s13, s18, s11
	s_lshl_b32 s6, s25, 19
	s_mov_b64 s[10:11], 0x1000

; #define LAS __attribute__((address_space(3)))
; __device__ __forceinline__ Cvb conv8b_dec(const Ctx& X, int bit) { Cvb c; int kb, nb;
;     if (bit < I_GU8 / 8) { const int e = bit >> 8, r = bit & 255; kb = r >> 4; nb = r & 15; c.N = 2 * DFF; c.W = XP_w_gu(X) + (size_t)e * D * (2 * DFF); c.WT = XP_WguT(X) + (size_t)e * 16 * PAN_GU + (size_t)kb * PAN_GU; }
;     else { const int b2 = bit - I_GU8 / 8, e = b2 >> 7, r = b2 & 127; kb = r >> 3; nb = r & 7; c.N = D; c.W = XP_w_d(X) + (size_t)e * DFF * D; c.WT = XP_WdT(X) + (size_t)e * 16 * PAN_D + (size_t)kb * PAN_D; }
;     c.W += (size_t)(kb * 128 + 16 * X.wave) * c.N + nb * 256 + 4 * X.lane;
;     c.WT += (size_t)(nb * 256 + 32 * X.wave + (X.lane >> 3)) * 128 + 16 * (X.lane & 7);
;     return c; }
; __device__ __forceinline__ void conv8b_run(const Ctx& X, int first, int step, int count) {
;     ...
;     for (int j = 0; j < count; ++j) {
;         LAS uchar* buf = X.lds + (j & 1) * CVT_BUF;
; #pragma unroll
;         for (int q = 0; q < 4; ++q) { u32x4 o;
;             o.x = pk_fp8x4(v[0][q] * W8_SCALE, v[1][q] * W8_SCALE, v[2][q] * W8_SCALE, v[3][q] * W8_SCALE); o.y = pk_fp8x4(v[4][q] * W8_SCALE, v[5][q] * W8_SCALE, v[6][q] * W8_SCALE, v[7][q] * W8_SCALE);
;             o.z = pk_fp8x4(v[8][q] * W8_SCALE, v[9][q] * W8_SCALE, v[10][q] * W8_SCALE, v[11][q] * W8_SCALE); o.w = pk_fp8x4(v[12][q] * W8_SCALE, v[13][q] * W8_SCALE, v[14][q] * W8_SCALE, v[15][q] * W8_SCALE);
;             *(LAS u32x4*)(buf + (4 * X.lane + q) * CVT_STRIDE + 16 * X.wave) = o; }
;         if (j + 1 < count) { cn = conv8b_dec(X, first + (j + 1) * step);
; #pragma unroll
;             for (int i = 0; i < 16; ++i) v[i] = __builtin_nontemporal_load((const f32x4*)(cn.W + (size_t)i * cn.N)); }
.LBB0_141:
	s_waitcnt vmcnt(4)
	v_mul_f32_e32 v83, 0x42800000, v2
	v_mul_f32_e32 v84, 0x42800000, v14
	v_med3_f32 v83, v83, s21, v82
	v_med3_f32 v86, v84, s21, v82
	v_mov_b32_e32 v84, 0
	v_cvt_pk_fp8_f32 v84, v83, v86
	v_mul_f32_e32 v85, 0x42800000, v6
	v_mul_f32_e32 v83, 0x42800000, v30
	v_med3_f32 v85, v85, s21, v82
	v_med3_f32 v83, v83, s21, v82
	v_cvt_pk_fp8_f32 v84, v85, v83 op_sel:[0,0,1]
	v_mul_f32_e32 v83, 0x42800000, v22
	v_mul_f32_e32 v85, 0x42800000, v46
	v_med3_f32 v83, v83, s21, v82
	v_med3_f32 v87, v85, s21, v82
	v_mov_b32_e32 v85, 0
	v_cvt_pk_fp8_f32 v85, v83, v87
	v_mul_f32_e32 v86, 0x42800000, v38
	v_mul_f32_e32 v83, 0x42800000, v50
	v_med3_f32 v86, v86, s21, v82
	v_med3_f32 v83, v83, s21, v82
	v_cvt_pk_fp8_f32 v85, v86, v83 op_sel:[0,0,1]
	v_mul_f32_e32 v83, 0x42800000, v54
	v_mul_f32_e32 v86, 0x42800000, v58
	v_med3_f32 v83, v83, s21, v82
	v_med3_f32 v88, v86, s21, v82
	v_mov_b32_e32 v86, 0
	v_cvt_pk_fp8_f32 v86, v83, v88
	v_mul_f32_e32 v87, 0x42800000, v42
	v_mul_f32_e32 v83, 0x42800000, v62
	v_med3_f32 v87, v87, s21, v82
	v_med3_f32 v83, v83, s21, v82
	v_cvt_pk_fp8_f32 v86, v87, v83 op_sel:[0,0,1]
	v_mul_f32_e32 v83, 0x42800000, v26
	v_mul_f32_e32 v87, 0x42800000, v34
	v_med3_f32 v83, v83, s21, v82
	v_med3_f32 v89, v87, s21, v82
	v_mov_b32_e32 v87, 0
	v_cvt_pk_fp8_f32 v87, v83, v89
	v_mul_f32_e32 v88, 0x42800000, v10
	v_mul_f32_e32 v83, 0x42800000, v18
	v_med3_f32 v88, v88, s21, v82
	v_med3_f32 v83, v83, s21, v82
	v_cvt_pk_fp8_f32 v87, v88, v83 op_sel:[0,0,1]
	v_mul_f32_e32 v83, 0x42800000, v3
	v_mul_f32_e32 v88, 0x42800000, v15
	v_med3_f32 v83, v83, s21, v82
	v_med3_f32 v90, v88, s21, v82
	v_mov_b32_e32 v88, 0
	v_cvt_pk_fp8_f32 v88, v83, v90
	v_mul_f32_e32 v89, 0x42800000, v7
	v_mul_f32_e32 v83, 0x42800000, v31
	v_med3_f32 v89, v89, s21, v82
	v_med3_f32 v83, v83, s21, v82
	v_cvt_pk_fp8_f32 v88, v89, v83 op_sel:[0,0,1]
	v_mul_f32_e32 v83, 0x42800000, v23
	v_mul_f32_e32 v89, 0x42800000, v47
	v_med3_f32 v83, v83, s21, v82
	v_med3_f32 v91, v89, s21, v82
	v_mov_b32_e32 v89, 0
	v_cvt_pk_fp8_f32 v89, v83, v91
	v_mul_f32_e32 v90, 0x42800000, v39
	v_mul_f32_e32 v83, 0x42800000, v51
	v_med3_f32 v90, v90, s21, v82
	v_med3_f32 v83, v83, s21, v82
	v_cvt_pk_fp8_f32 v89, v90, v83 op_sel:[0,0,1]
	v_mul_f32_e32 v83, 0x42800000, v55
	v_mul_f32_e32 v90, 0x42800000, v59
	v_med3_f32 v83, v83, s21, v82
	v_med3_f32 v92, v90, s21, v82
	v_mov_b32_e32 v90, 0
	v_cvt_pk_fp8_f32 v90, v83, v92
	v_mul_f32_e32 v91, 0x42800000, v43
	v_mul_f32_e32 v83, 0x42800000, v63
	v_med3_f32 v91, v91, s21, v82
	v_med3_f32 v83, v83, s21, v82
	v_cvt_pk_fp8_f32 v90, v91, v83 op_sel:[0,0,1]
	v_mul_f32_e32 v83, 0x42800000, v27
	v_mul_f32_e32 v91, 0x42800000, v35
	v_med3_f32 v83, v83, s21, v82
	v_med3_f32 v93, v91, s21, v82
	v_mov_b32_e32 v91, 0
	v_cvt_pk_fp8_f32 v91, v83, v93
	s_bitcmp1_b32 s6, 0
	v_mul_f32_e32 v92, 0x42800000, v11
	v_mul_f32_e32 v83, 0x42800000, v19
	s_cselect_b32 s8, 0x9000, 0
	v_med3_f32 v92, v92, s21, v82
	v_med3_f32 v83, v83, s21, v82
	s_add_i32 s24, s8, 0
	v_cvt_pk_fp8_f32 v91, v92, v83 op_sel:[0,0,1]
	s_add_i32 s8, s19, s24
	v_add_u32_e32 v83, s8, v78
	ds_write_b128 v83, v[84:87]
	ds_write_b128 v83, v[88:91] offset:144
	v_mul_f32_e32 v84, 0x42800000, v4
	v_mul_f32_e32 v85, 0x42800000, v16
	v_med3_f32 v87, v84, s21, v82
	v_med3_f32 v85, v85, s21, v82
	v_mov_b32_e32 v84, 0
	v_cvt_pk_fp8_f32 v84, v87, v85
	v_mul_f32_e32 v86, 0x42800000, v8
	v_mul_f32_e32 v85, 0x42800000, v32
	v_med3_f32 v86, v86, s21, v82
	v_med3_f32 v85, v85, s21, v82
	v_cvt_pk_fp8_f32 v84, v86, v85 op_sel:[0,0,1]
	v_mul_f32_e32 v85, 0x42800000, v24
	v_mul_f32_e32 v86, 0x42800000, v48
	v_med3_f32 v88, v85, s21, v82
	v_med3_f32 v86, v86, s21, v82
	v_mov_b32_e32 v85, 0
	v_cvt_pk_fp8_f32 v85, v88, v86
	v_mul_f32_e32 v87, 0x42800000, v40
	v_mul_f32_e32 v86, 0x42800000, v52
	v_med3_f32 v87, v87, s21, v82
	v_med3_f32 v86, v86, s21, v82
	v_cvt_pk_fp8_f32 v85, v87, v86 op_sel:[0,0,1]
	v_mul_f32_e32 v86, 0x42800000, v56
	v_mul_f32_e32 v87, 0x42800000, v60
	v_med3_f32 v89, v86, s21, v82
	v_med3_f32 v87, v87, s21, v82
	v_mov_b32_e32 v86, 0
	v_cvt_pk_fp8_f32 v86, v89, v87
	v_mul_f32_e32 v88, 0x42800000, v44
	v_mul_f32_e32 v87, 0x42800000, v64
	v_med3_f32 v88, v88, s21, v82
	v_med3_f32 v87, v87, s21, v82
	v_cvt_pk_fp8_f32 v86, v88, v87 op_sel:[0,0,1]
	v_mul_f32_e32 v87, 0x42800000, v28
	v_mul_f32_e32 v88, 0x42800000, v36
	v_med3_f32 v90, v87, s21, v82
	v_med3_f32 v88, v88, s21, v82
	v_mov_b32_e32 v87, 0
	v_cvt_pk_fp8_f32 v87, v90, v88
	v_mul_f32_e32 v89, 0x42800000, v12
	v_mul_f32_e32 v88, 0x42800000, v20
	v_med3_f32 v89, v89, s21, v82
	v_med3_f32 v88, v88, s21, v82
	v_cvt_pk_fp8_f32 v87, v89, v88 op_sel:[0,0,1]
	v_mul_f32_e32 v88, 0x42800000, v5
	v_mul_f32_e32 v89, 0x42800000, v17
	v_med3_f32 v91, v88, s21, v82
	v_med3_f32 v89, v89, s21, v82
	v_mov_b32_e32 v88, 0
	v_cvt_pk_fp8_f32 v88, v91, v89
	v_mul_f32_e32 v90, 0x42800000, v9
	v_mul_f32_e32 v89, 0x42800000, v33
	v_med3_f32 v90, v90, s21, v82
	v_med3_f32 v89, v89, s21, v82
	v_cvt_pk_fp8_f32 v88, v90, v89 op_sel:[0,0,1]
	v_mul_f32_e32 v89, 0x42800000, v25
	v_mul_f32_e32 v90, 0x42800000, v49
	v_med3_f32 v92, v89, s21, v82
	v_med3_f32 v90, v90, s21, v82
	v_mov_b32_e32 v89, 0
	v_cvt_pk_fp8_f32 v89, v92, v90
	v_mul_f32_e32 v91, 0x42800000, v41
	v_mul_f32_e32 v90, 0x42800000, v53
	v_med3_f32 v91, v91, s21, v82
	v_med3_f32 v90, v90, s21, v82
	v_cvt_pk_fp8_f32 v89, v91, v90 op_sel:[0,0,1]
	v_mul_f32_e32 v90, 0x42800000, v57
	v_mul_f32_e32 v91, 0x42800000, v61
	v_med3_f32 v93, v90, s21, v82
	v_med3_f32 v91, v91, s21, v82
	v_mov_b32_e32 v90, 0
	v_cvt_pk_fp8_f32 v90, v93, v91
	v_mul_f32_e32 v92, 0x42800000, v45
	v_mul_f32_e32 v91, 0x42800000, v65
	v_med3_f32 v92, v92, s21, v82
	v_med3_f32 v91, v91, s21, v82
	v_cvt_pk_fp8_f32 v90, v92, v91 op_sel:[0,0,1]
	v_mul_f32_e32 v91, 0x42800000, v29
	v_mul_f32_e32 v92, 0x42800000, v37
	v_med3_f32 v94, v91, s21, v82
	v_med3_f32 v92, v92, s21, v82
	v_mov_b32_e32 v91, 0
	v_cvt_pk_fp8_f32 v91, v94, v92
	v_mul_f32_e32 v93, 0x42800000, v13
	v_mul_f32_e32 v92, 0x42800000, v21
	v_med3_f32 v93, v93, s21, v82
	v_med3_f32 v92, v92, s21, v82
	v_cvt_pk_fp8_f32 v91, v93, v92 op_sel:[0,0,1]
	s_add_i32 s25, s6, 1
	s_cmp_ge_i32 s25, s23
	ds_write_b128 v83, v[84:87] offset:288
	ds_write_b128 v83, v[88:91] offset:432
	s_cbranch_scc1 .LBB0_140
	s_add_i32 s29, s22, s6
	s_add_i32 s28, s29, 1
	s_cmpk_gt_i32 s28, 0x1fff
	s_mov_b64 s[12:13], -1
	s_cbranch_scc0 .LBB0_144
	s_mov_b64 s[8:9], s[100:101]
	s_addk_i32 s29, 0xe001
	s_lshr_b32 s6, s29, 7
	s_bfe_u32 s27, s28, 0x40003
	s_and_b32 s26, s28, 7
	s_lshl_b64 s[10:11], s[6:7], 24
	s_waitcnt lgkmcnt(0)
	s_add_u32 s8, s8, s10
	s_addc_u32 s9, s9, s11
	s_lshl_b64 s[10:11], s[6:7], 22
	s_add_u32 s10, s15, s10
	s_addc_u32 s11, s16, s11
	s_lshl_b32 s6, s27, 18
	s_mov_b64 s[12:13], 0
; __device__ __forceinline__ Cvb conv8b_dec(const Ctx& X, int bit) { Cvb c; int kb, nb;
;     if (bit < I_GU8 / 8) { const int e = bit >> 8, r = bit & 255; kb = r >> 4; nb = r & 15; c.N = 2 * DFF; c.W = XP_w_gu(X) + (size_t)e * D * (2 * DFF); c.WT = XP_WguT(X) + (size_t)e * 16 * PAN_GU + (size_t)kb * PAN_GU; }
;     else { const int b2 = bit - I_GU8 / 8, e = b2 >> 7, r = b2 & 127; kb = r >> 3; nb = r & 7; c.N = D; c.W = XP_w_d(X) + (size_t)e * DFF * D; c.WT = XP_WdT(X) + (size_t)e * 16 * PAN_D + (size_t)kb * PAN_D; }
;     c.W += (size_t)(kb * 128 + 16 * X.wave) * c.N + nb * 256 + 4 * X.lane;
;     c.WT += (size_t)(nb * 256 + 32 * X.wave + (X.lane >> 3)) * 128 + 16 * (X.lane & 7);
;     return c; }
.LBB0_144:
	s_andn2_b64 vcc, exec, s[12:13]
	s_mov_b64 s[12:13], 0x800
	s_cbranch_vccnz .LBB0_139
	s_mov_b64 s[8:9], s[98:99]
	s_ashr_i32 s10, s28, 8
	s_ashr_i32 s11, s10, 31
	s_bfe_u32 s27, s28, 0x40004
	s_and_b32 s26, s28, 15
	s_lshl_b64 s[12:13], s[10:11], 25
	s_waitcnt lgkmcnt(0)
	s_add_u32 s8, s8, s12
	s_addc_u32 s9, s9, s13
	s_lshl_b64 s[10:11], s[10:11], 23
	s_add_u32 s10, s17, s10
	s_addc_u32 s11, s18, s11
	s_lshl_b32 s6, s27, 19
	s_mov_b64 s[12:13], 0x1000
	s_branch .LBB0_139

; __device__ __forceinline__ void conv8_fill(const Ctx& X, int base, int rank, int nblk, int n) { conv8b_run(X, (base >> 3) + rank, nblk, n); }
; #define SEAM(k) do { if (IN(k) && IN((k) + 1)) xcd_barrier(bar); } while (0)
; __device__ __forceinline__ Cvb conv8b_dec(const Ctx& X, int bit) { Cvb c; int kb, nb;
;     if (bit < I_GU8 / 8) { const int e = bit >> 8, r = bit & 255; kb = r >> 4; nb = r & 15; c.N = 2 * DFF; c.W = XP_w_gu(X) + (size_t)e * D * (2 * DFF); c.WT = XP_WguT(X) + (size_t)e * 16 * PAN_GU + (size_t)kb * PAN_GU; }
;     else { const int b2 = bit - I_GU8 / 8, e = b2 >> 7, r = b2 & 127; kb = r >> 3; nb = r & 7; c.N = D; c.W = XP_w_d(X) + (size_t)e * DFF * D; c.WT = XP_WdT(X) + (size_t)e * 16 * PAN_D + (size_t)kb * PAN_D; }
;     c.W += (size_t)(kb * 128 + 16 * X.wave) * c.N + nb * 256 + 4 * X.lane;
;     c.WT += (size_t)(nb * 256 + 32 * X.wave + (X.lane >> 3)) * 128 + 16 * (X.lane & 7);
;     return c; }
; __device__ __forceinline__ void conv8b_run(const Ctx& X, int first, int step, int count) {
;     if (count <= 0) return;
;     f32x4 v[16];
;     Cvb c = conv8b_dec(X, first), cn = c;
; #pragma unroll
;     for (int i = 0; i < 16; ++i) v[i] = __builtin_nontemporal_load((const f32x4*)(c.W + (size_t)i * c.N));
; __global__ void __launch_bounds__(NTHR, 2) fwd(Args args) {
;     ...
;     if (IN(3)) { p3_scan(X); if (X.G == 256 && X.bid >= 192) conv8_fill(X, FILL_B3, X.bid - 192, FILL_W3 / NWAVES, FILL_N3); } SEAM(3);
.LBB0_474:
	s_or_b64 exec, exec, s[6:7]
	s_cmpk_lg_i32 s92, 0x100
	s_cselect_b64 s[2:3], -1, 0
	s_cmpk_lt_i32 s87, 0xc0
	s_cselect_b64 s[6:7], -1, 0
	s_or_b64 s[2:3], s[6:7], s[2:3]
	s_and_b64 vcc, exec, s[2:3]
	s_cbranch_vccnz .LBB0_480
	s_load_dwordx2 s[6:7], s[0:1], 0x80
	s_add_i32 s2, s87, 0x900
	s_lshr_b32 s2, s2, 7
	s_mov_b32 s3, 0
	s_bfe_u32 s13, s87, 0x40003
	s_lshl_b64 s[8:9], s[2:3], 24
	s_waitcnt lgkmcnt(0)
	s_mov_b64 s[100:101], s[6:7]
	s_add_u32 s14, s6, s8
	s_addc_u32 s15, s7, s9
	s_add_u32 s10, s90, 0x50000000
	s_addc_u32 s11, s91, 0
	s_lshl_b64 s[6:7], s[2:3], 22
	s_add_u32 s2, s10, s6
	s_addc_u32 s7, s11, s7
	s_lshl_b32 s6, s13, 18
	s_add_u32 s6, s2, s6
	s_addc_u32 s7, s7, 0
	s_lshl_b32 s2, s87, 8
	s_lshl_b32 s16, s93, 5
	s_and_b32 s17, s2, 0x700
	s_add_i32 s2, s16, s17
	v_lshrrev_b32_e32 v75, 3, v194
	v_or_b32_e32 v66, s2, v75
	s_lshl_b32 s12, s93, 4
	s_lshl_b32 s2, s13, 7
	s_add_i32 s2, s12, s2
	s_lshl_b64 s[8:9], s[2:3], 13
	s_add_u32 s2, s14, s8
	s_addc_u32 s9, s15, s9
	s_lshl_b32 s8, s17, 2
	v_mov_b32_e32 v67, 0
	s_add_u32 s8, s2, s8
	v_lshlrev_b64 v[68:69], 7, v[66:67]
	s_addc_u32 s9, s9, 0
	v_lshlrev_b32_e32 v66, 4, v194
	s_waitcnt vmcnt(3)
	v_lshl_add_u64 v[30:31], s[8:9], 0, v[66:67]
	s_mov_b32 s2, 0x1e000
	v_add_co_u32_e32 v6, vcc, s2, v30
	s_mov_b32 s2, 0x1c000
	s_nop 0
	v_addc_co_u32_e32 v7, vcc, 0, v31, vcc
	v_add_co_u32_e32 v8, vcc, s2, v30
	s_mov_b32 s2, 0x1a000
	s_nop 0
	v_addc_co_u32_e32 v9, vcc, 0, v31, vcc
	v_add_co_u32_e32 v10, vcc, s2, v30
	s_mov_b32 s2, 0x18000
	s_nop 0
	v_addc_co_u32_e32 v11, vcc, 0, v31, vcc
	v_add_co_u32_e32 v12, vcc, s2, v30
	s_mov_b32 s2, 0x16000
	s_nop 0
	v_addc_co_u32_e32 v13, vcc, 0, v31, vcc
	v_add_co_u32_e32 v14, vcc, s2, v30
	s_mov_b32 s2, 0x14000
	s_nop 0
	v_addc_co_u32_e32 v15, vcc, 0, v31, vcc
	v_add_co_u32_e32 v16, vcc, s2, v30
	s_mov_b32 s2, 0x12000
	s_nop 0
	v_addc_co_u32_e32 v17, vcc, 0, v31, vcc
	v_add_co_u32_e32 v18, vcc, s2, v30
	s_mov_b32 s2, 0x10000
	s_nop 0
	v_addc_co_u32_e32 v19, vcc, 0, v31, vcc
	v_add_co_u32_e32 v20, vcc, s2, v30
	s_mov_b32 s2, 0xe000
	s_nop 0
	v_addc_co_u32_e32 v21, vcc, 0, v31, vcc
	v_add_co_u32_e32 v22, vcc, s2, v30
	s_mov_b32 s2, 0xc000
	s_nop 0
	v_addc_co_u32_e32 v23, vcc, 0, v31, vcc
	v_add_co_u32_e32 v24, vcc, s2, v30
	s_mov_b32 s2, 0xa000
	s_nop 0
	v_addc_co_u32_e32 v25, vcc, 0, v31, vcc
	v_add_co_u32_e32 v26, vcc, s2, v30
	s_mov_b32 s2, 0x8000
	s_nop 0
	v_addc_co_u32_e32 v27, vcc, 0, v31, vcc
	v_add_co_u32_e32 v28, vcc, s2, v30
	s_movk_i32 s2, 0x6000
	s_nop 0
	v_addc_co_u32_e32 v29, vcc, 0, v31, vcc
	v_add_co_u32_e32 v32, vcc, s2, v30
	s_movk_i32 s2, 0x4000
	s_nop 0
	v_addc_co_u32_e32 v33, vcc, 0, v31, vcc
	s_waitcnt vmcnt(0)
	v_add_co_u32_e32 v62, vcc, s2, v30
	s_movk_i32 s2, 0x2000
	s_nop 0
	v_addc_co_u32_e32 v63, vcc, 0, v31, vcc
	v_add_co_u32_e32 v70, vcc, s2, v30
	global_load_dwordx4 v[34:37], v[6:7], off nt
	global_load_dwordx4 v[2:5], v[8:9], off nt
	v_addc_co_u32_e32 v71, vcc, 0, v31, vcc
	global_load_dwordx4 v[38:41], v[10:11], off nt
	global_load_dwordx4 v[6:9], v[12:13], off nt
	global_load_dwordx4 v[42:45], v[14:15], off nt
	s_nop 0
	global_load_dwordx4 v[10:13], v[16:17], off nt
	global_load_dwordx4 v[46:49], v[18:19], off nt
	s_nop 0
	global_load_dwordx4 v[14:17], v[20:21], off nt
	global_load_dwordx4 v[50:53], v[22:23], off nt
	s_nop 0
	global_load_dwordx4 v[18:21], v[24:25], off nt
	global_load_dwordx4 v[54:57], v[26:27], off nt
	s_nop 0
	global_load_dwordx4 v[22:25], v[28:29], off nt
	global_load_dwordx4 v[58:61], v[32:33], off nt
	s_nop 0
	global_load_dwordx4 v[26:29], v[62:63], off nt
	global_load_dwordx4 v[30:33], v[70:71], off nt
	s_nop 0
	global_load_dwordx4 v[62:65], v66, s[8:9] nt
	v_lshlrev_b32_e32 v66, 4, v0
	v_lshl_add_u64 v[70:71], s[6:7], 0, v[68:69]
	v_and_b32_e32 v68, 0x70, v66
	v_mov_b32_e32 v69, v67
	v_or_b32_e32 v66, s16, v75
	s_movk_i32 s2, 0x90
	v_lshl_add_u64 v[72:73], v[70:71], 0, v[68:69]
	v_lshlrev_b32_e32 v74, 2, v194
	v_mul_lo_u32 v77, v66, s2
	v_add_u32_e32 v66, s17, v66
	v_mul_u32_u24_e32 v76, 0x240, v194
	v_lshlrev_b64 v[70:71], 7, v[66:67]
	s_add_i32 s13, s87, 0x2940
	s_mov_b32 s14, 0xc3e00000
	s_lshl_b32 s15, s17, 2
	v_lshlrev_b32_e32 v66, 2, v74
	v_mov_b32_e32 v78, 0x43e00000
	s_mov_b32 s16, 0
	v_mov_b64_e32 v[74:75], v[72:73]
	s_waitcnt vmcnt(0)
	s_branch .LBB0_477

; #define LAS __attribute__((address_space(3)))
; __device__ __forceinline__ void conv8b_run(const Ctx& X, int first, int step, int count) {
;     ...
;         LAS uchar* buf = X.lds + (j & 1) * CVT_BUF;
; #pragma unroll
;         for (int q = 0; q < 4; ++q) { u32x4 o;
;             o.x = pk_fp8x4(v[0][q] * W8_SCALE, v[1][q] * W8_SCALE, v[2][q] * W8_SCALE, v[3][q] * W8_SCALE); o.y = pk_fp8x4(v[4][q] * W8_SCALE, v[5][q] * W8_SCALE, v[6][q] * W8_SCALE, v[7][q] * W8_SCALE);
;             o.z = pk_fp8x4(v[8][q] * W8_SCALE, v[9][q] * W8_SCALE, v[10][q] * W8_SCALE, v[11][q] * W8_SCALE); o.w = pk_fp8x4(v[12][q] * W8_SCALE, v[13][q] * W8_SCALE, v[14][q] * W8_SCALE, v[15][q] * W8_SCALE);
;             *(LAS u32x4*)(buf + (4 * X.lane + q) * CVT_STRIDE + 16 * X.wave) = o; }
.LBB0_477:
	s_waitcnt vmcnt(4)
	v_mul_f32_e32 v79, 0x42800000, v62
	v_mul_f32_e32 v80, 0x42800000, v30
	v_med3_f32 v79, v79, s14, v78
	v_med3_f32 v82, v80, s14, v78
	v_mov_b32_e32 v80, 0
	v_cvt_pk_fp8_f32 v80, v79, v82
	v_mul_f32_e32 v81, 0x42800000, v26
	v_mul_f32_e32 v79, 0x42800000, v58
	v_med3_f32 v81, v81, s14, v78
	v_med3_f32 v79, v79, s14, v78
	v_cvt_pk_fp8_f32 v80, v81, v79 op_sel:[0,0,1]
	v_mul_f32_e32 v79, 0x42800000, v22
	v_mul_f32_e32 v81, 0x42800000, v54
	v_med3_f32 v79, v79, s14, v78
	v_med3_f32 v83, v81, s14, v78
	v_mov_b32_e32 v81, 0
	v_cvt_pk_fp8_f32 v81, v79, v83
	v_mul_f32_e32 v82, 0x42800000, v18
	v_mul_f32_e32 v79, 0x42800000, v50
	v_med3_f32 v82, v82, s14, v78
	v_med3_f32 v79, v79, s14, v78
	v_cvt_pk_fp8_f32 v81, v82, v79 op_sel:[0,0,1]
	v_mul_f32_e32 v79, 0x42800000, v14
	v_mul_f32_e32 v82, 0x42800000, v46
	v_med3_f32 v79, v79, s14, v78
	v_med3_f32 v84, v82, s14, v78
	v_mov_b32_e32 v82, 0
	v_cvt_pk_fp8_f32 v82, v79, v84
	v_mul_f32_e32 v83, 0x42800000, v10
	v_mul_f32_e32 v79, 0x42800000, v42
	v_med3_f32 v83, v83, s14, v78
	v_med3_f32 v79, v79, s14, v78
	v_cvt_pk_fp8_f32 v82, v83, v79 op_sel:[0,0,1]
	v_mul_f32_e32 v79, 0x42800000, v6
	v_mul_f32_e32 v83, 0x42800000, v38
	v_med3_f32 v79, v79, s14, v78
	v_med3_f32 v85, v83, s14, v78
	v_mov_b32_e32 v83, 0
	v_cvt_pk_fp8_f32 v83, v79, v85
	v_mul_f32_e32 v84, 0x42800000, v2
	v_mul_f32_e32 v79, 0x42800000, v34
	s_bitcmp1_b32 s16, 0
	v_med3_f32 v84, v84, s14, v78
	v_med3_f32 v79, v79, s14, v78
	s_cselect_b32 s2, 0x9000, 0
	v_cvt_pk_fp8_f32 v83, v84, v79 op_sel:[0,0,1]
	s_add_i32 s17, s2, 0
	s_add_i32 s2, s12, s17
	v_add_u32_e32 v79, s2, v76
	ds_write_b128 v79, v[80:83]
	v_mul_f32_e32 v80, 0x42800000, v63
	v_mul_f32_e32 v81, 0x42800000, v31
	v_med3_f32 v83, v80, s14, v78
	v_med3_f32 v81, v81, s14, v78
	v_mov_b32_e32 v80, 0
	v_cvt_pk_fp8_f32 v80, v83, v81
	v_mul_f32_e32 v82, 0x42800000, v27
	v_mul_f32_e32 v81, 0x42800000, v59
	v_med3_f32 v82, v82, s14, v78
	v_med3_f32 v81, v81, s14, v78
	v_cvt_pk_fp8_f32 v80, v82, v81 op_sel:[0,0,1]
	v_mul_f32_e32 v81, 0x42800000, v23
	v_mul_f32_e32 v82, 0x42800000, v55
	v_med3_f32 v84, v81, s14, v78
	v_med3_f32 v82, v82, s14, v78
	v_mov_b32_e32 v81, 0
	v_cvt_pk_fp8_f32 v81, v84, v82
	v_mul_f32_e32 v83, 0x42800000, v19
	v_mul_f32_e32 v82, 0x42800000, v51
	v_med3_f32 v83, v83, s14, v78
	v_med3_f32 v82, v82, s14, v78
	v_cvt_pk_fp8_f32 v81, v83, v82 op_sel:[0,0,1]
	v_mul_f32_e32 v82, 0x42800000, v15
	v_mul_f32_e32 v83, 0x42800000, v47
	v_med3_f32 v85, v82, s14, v78
	v_med3_f32 v83, v83, s14, v78
	v_mov_b32_e32 v82, 0
	v_cvt_pk_fp8_f32 v82, v85, v83
	v_mul_f32_e32 v84, 0x42800000, v11
	v_mul_f32_e32 v83, 0x42800000, v43
	v_med3_f32 v84, v84, s14, v78
	v_med3_f32 v83, v83, s14, v78
	v_cvt_pk_fp8_f32 v82, v84, v83 op_sel:[0,0,1]
	v_mul_f32_e32 v83, 0x42800000, v7
	v_mul_f32_e32 v84, 0x42800000, v39
	v_med3_f32 v86, v83, s14, v78
	v_med3_f32 v84, v84, s14, v78
	v_mov_b32_e32 v83, 0
	v_cvt_pk_fp8_f32 v83, v86, v84
	v_mul_f32_e32 v85, 0x42800000, v3
	v_mul_f32_e32 v84, 0x42800000, v35
	v_med3_f32 v85, v85, s14, v78
	v_med3_f32 v84, v84, s14, v78
	v_cvt_pk_fp8_f32 v83, v85, v84 op_sel:[0,0,1]
	v_mul_f32_e32 v84, 0x42800000, v64
	v_mul_f32_e32 v85, 0x42800000, v32
	v_med3_f32 v87, v84, s14, v78
	v_med3_f32 v85, v85, s14, v78
	v_mov_b32_e32 v84, 0
	v_cvt_pk_fp8_f32 v84, v87, v85
	v_mul_f32_e32 v86, 0x42800000, v28
	v_mul_f32_e32 v85, 0x42800000, v60
	v_med3_f32 v86, v86, s14, v78
	v_med3_f32 v85, v85, s14, v78
	v_cvt_pk_fp8_f32 v84, v86, v85 op_sel:[0,0,1]
	v_mul_f32_e32 v85, 0x42800000, v24
	v_mul_f32_e32 v86, 0x42800000, v56
	v_med3_f32 v88, v85, s14, v78
	v_med3_f32 v86, v86, s14, v78
	v_mov_b32_e32 v85, 0
	v_cvt_pk_fp8_f32 v85, v88, v86
	v_mul_f32_e32 v87, 0x42800000, v20
	v_mul_f32_e32 v86, 0x42800000, v52
	v_med3_f32 v87, v87, s14, v78
	v_med3_f32 v86, v86, s14, v78
	v_cvt_pk_fp8_f32 v85, v87, v86 op_sel:[0,0,1]
	v_mul_f32_e32 v86, 0x42800000, v16
	v_mul_f32_e32 v87, 0x42800000, v48
	v_med3_f32 v89, v86, s14, v78
	v_med3_f32 v87, v87, s14, v78
	v_mov_b32_e32 v86, 0
	v_cvt_pk_fp8_f32 v86, v89, v87
	v_mul_f32_e32 v88, 0x42800000, v12
	v_mul_f32_e32 v87, 0x42800000, v44
	v_med3_f32 v88, v88, s14, v78
	v_med3_f32 v87, v87, s14, v78
	v_cvt_pk_fp8_f32 v86, v88, v87 op_sel:[0,0,1]
	v_mul_f32_e32 v87, 0x42800000, v8
	v_mul_f32_e32 v88, 0x42800000, v40
	v_med3_f32 v90, v87, s14, v78
	v_med3_f32 v88, v88, s14, v78
	v_mov_b32_e32 v87, 0
	v_cvt_pk_fp8_f32 v87, v90, v88
	v_mul_f32_e32 v89, 0x42800000, v4
	v_mul_f32_e32 v88, 0x42800000, v36
	v_med3_f32 v89, v89, s14, v78
	v_med3_f32 v88, v88, s14, v78
	v_cvt_pk_fp8_f32 v87, v89, v88 op_sel:[0,0,1]
	v_mul_f32_e32 v88, 0x42800000, v65
	v_mul_f32_e32 v89, 0x42800000, v33
	v_med3_f32 v91, v88, s14, v78
	v_med3_f32 v89, v89, s14, v78
	v_mov_b32_e32 v88, 0
	v_cvt_pk_fp8_f32 v88, v91, v89
	v_mul_f32_e32 v90, 0x42800000, v29
	v_mul_f32_e32 v89, 0x42800000, v61
	v_med3_f32 v90, v90, s14, v78
	v_med3_f32 v89, v89, s14, v78
	v_cvt_pk_fp8_f32 v88, v90, v89 op_sel:[0,0,1]
	v_mul_f32_e32 v89, 0x42800000, v25
	v_mul_f32_e32 v90, 0x42800000, v57
	v_med3_f32 v92, v89, s14, v78
	v_med3_f32 v90, v90, s14, v78
	v_mov_b32_e32 v89, 0
	v_cvt_pk_fp8_f32 v89, v92, v90
	v_mul_f32_e32 v91, 0x42800000, v21
	v_mul_f32_e32 v90, 0x42800000, v53
	v_med3_f32 v91, v91, s14, v78
	v_med3_f32 v90, v90, s14, v78
	v_cvt_pk_fp8_f32 v89, v91, v90 op_sel:[0,0,1]
	v_mul_f32_e32 v90, 0x42800000, v17
	v_mul_f32_e32 v91, 0x42800000, v49
	v_med3_f32 v93, v90, s14, v78
	v_med3_f32 v91, v91, s14, v78
	v_mov_b32_e32 v90, 0
	v_cvt_pk_fp8_f32 v90, v93, v91
	v_mul_f32_e32 v92, 0x42800000, v13
	v_mul_f32_e32 v91, 0x42800000, v45
	v_med3_f32 v92, v92, s14, v78
	v_med3_f32 v91, v91, s14, v78
	v_cvt_pk_fp8_f32 v90, v92, v91 op_sel:[0,0,1]
	v_mul_f32_e32 v91, 0x42800000, v9
	v_mul_f32_e32 v92, 0x42800000, v41
	v_med3_f32 v94, v91, s14, v78
	v_med3_f32 v92, v92, s14, v78
	v_mov_b32_e32 v91, 0
	v_cvt_pk_fp8_f32 v91, v94, v92
	v_mul_f32_e32 v93, 0x42800000, v5
	v_mul_f32_e32 v92, 0x42800000, v37
	v_med3_f32 v93, v93, s14, v78
	v_med3_f32 v92, v92, s14, v78
	v_cvt_pk_fp8_f32 v91, v93, v92 op_sel:[0,0,1]
	s_cmp_gt_u32 s16, 1
	ds_write_b128 v79, v[80:83] offset:144
	ds_write_b128 v79, v[84:87] offset:288
	ds_write_b128 v79, v[88:91] offset:432
	s_cbranch_scc1 .LBB0_476
; __device__ __forceinline__ Cvb conv8b_dec(const Ctx& X, int bit) { Cvb c; int kb, nb;
;     if (bit < I_GU8 / 8) { const int e = bit >> 8, r = bit & 255; kb = r >> 4; nb = r & 15; c.N = 2 * DFF; c.W = XP_w_gu(X) + (size_t)e * D * (2 * DFF); c.WT = XP_WguT(X) + (size_t)e * 16 * PAN_GU + (size_t)kb * PAN_GU; }
;     else { const int b2 = bit - I_GU8 / 8, e = b2 >> 7, r = b2 & 127; kb = r >> 3; nb = r & 7; c.N = D; c.W = XP_w_d(X) + (size_t)e * DFF * D; c.WT = XP_WdT(X) + (size_t)e * 16 * PAN_D + (size_t)kb * PAN_D; }
;     c.W += (size_t)(kb * 128 + 16 * X.wave) * c.N + nb * 256 + 4 * X.lane;
;     c.WT += (size_t)(nb * 256 + 32 * X.wave + (X.lane >> 3)) * 128 + 16 * (X.lane & 7);
;     return c; }
; __device__ __forceinline__ void conv8b_run(const Ctx& X, int first, int step, int count) {
;     ...
;         if (j + 1 < count) { cn = conv8b_dec(X, first + (j + 1) * step);
; #pragma unroll
;             for (int i = 0; i < 16; ++i) v[i] = __builtin_nontemporal_load((const f32x4*)(cn.W + (size_t)i * cn.N)); }
	s_add_i32 s2, s13, 0xffffe000
	s_mov_b64 s[6:7], s[100:101]
	s_bfe_u32 s18, s13, 0x40003
	s_lshr_b32 s2, s2, 7
	s_lshl_b32 s19, s18, 18
	s_lshl_b64 s[8:9], s[2:3], 22
	s_add_u32 s20, s10, s8
	s_addc_u32 s21, s11, s9
	s_lshl_b64 s[8:9], s[2:3], 24
	s_waitcnt lgkmcnt(0)
	s_add_u32 s22, s6, s8
	s_addc_u32 s23, s7, s9
	s_add_u32 s6, s20, s19
	s_addc_u32 s7, s21, 0
	s_lshl_b32 s2, s18, 7
	s_add_i32 s2, s2, s12
	s_lshl_b64 s[8:9], s[2:3], 13
	s_add_u32 s2, s22, s8
	s_addc_u32 s9, s23, s9
	s_add_u32 s8, s2, s15
	s_addc_u32 s9, s9, 0
	v_lshl_add_u64 v[34:35], s[8:9], 0, v[66:67]
	v_add_co_u32_e32 v2, vcc, 0x2000, v34
	s_nop 1
	v_addc_co_u32_e32 v3, vcc, 0, v35, vcc
	v_add_co_u32_e32 v4, vcc, 0x4000, v34
	s_nop 1
	v_addc_co_u32_e32 v5, vcc, 0, v35, vcc
	global_load_dwordx4 v[30:33], v[2:3], off nt
	global_load_dwordx4 v[26:29], v[4:5], off nt
	v_add_co_u32_e32 v2, vcc, 0x6000, v34
	s_nop 1
	v_addc_co_u32_e32 v3, vcc, 0, v35, vcc
	v_add_co_u32_e32 v4, vcc, 0x8000, v34
	s_nop 1
	v_addc_co_u32_e32 v5, vcc, 0, v35, vcc
	global_load_dwordx4 v[58:61], v[2:3], off nt
	global_load_dwordx4 v[22:25], v[4:5], off nt
	v_add_co_u32_e32 v2, vcc, 0xa000, v34
	s_nop 1
	v_addc_co_u32_e32 v3, vcc, 0, v35, vcc
	v_add_co_u32_e32 v4, vcc, 0xc000, v34
	s_nop 1
	v_addc_co_u32_e32 v5, vcc, 0, v35, vcc
	global_load_dwordx4 v[54:57], v[2:3], off nt
	global_load_dwordx4 v[18:21], v[4:5], off nt
	v_add_co_u32_e32 v2, vcc, 0xe000, v34
	s_nop 1
	v_addc_co_u32_e32 v3, vcc, 0, v35, vcc
	v_add_co_u32_e32 v4, vcc, 0x10000, v34
	s_nop 1
	v_addc_co_u32_e32 v5, vcc, 0, v35, vcc
	global_load_dwordx4 v[50:53], v[2:3], off nt
	global_load_dwordx4 v[14:17], v[4:5], off nt
	v_add_co_u32_e32 v2, vcc, 0x12000, v34
	s_nop 1
	v_addc_co_u32_e32 v3, vcc, 0, v35, vcc
	v_add_co_u32_e32 v4, vcc, 0x14000, v34
	s_nop 1
	v_addc_co_u32_e32 v5, vcc, 0, v35, vcc
	global_load_dwordx4 v[46:49], v[2:3], off nt
	global_load_dwordx4 v[10:13], v[4:5], off nt
	v_add_co_u32_e32 v2, vcc, 0x16000, v34
	s_nop 1
	v_addc_co_u32_e32 v3, vcc, 0, v35, vcc
	v_add_co_u32_e32 v4, vcc, 0x18000, v34
	s_nop 1
	v_addc_co_u32_e32 v5, vcc, 0, v35, vcc
	v_add_co_u32_e32 v36, vcc, 0x1a000, v34
	global_load_dwordx4 v[42:45], v[2:3], off nt
	global_load_dwordx4 v[6:9], v[4:5], off nt
	v_addc_co_u32_e32 v37, vcc, 0, v35, vcc
	v_add_co_u32_e32 v62, vcc, 0x1c000, v34
	s_nop 1
	v_addc_co_u32_e32 v63, vcc, 0, v35, vcc
	v_add_co_u32_e32 v74, vcc, 0x1e000, v34
	global_load_dwordx4 v[38:41], v[36:37], off nt
	global_load_dwordx4 v[2:5], v[62:63], off nt
	v_addc_co_u32_e32 v75, vcc, 0, v35, vcc
	global_load_dwordx4 v[62:65], v66, s[8:9] nt
	global_load_dwordx4 v[34:37], v[74:75], off nt
	v_lshl_add_u64 v[74:75], s[6:7], 0, v[70:71]
	v_lshl_add_u64 v[74:75], v[74:75], 0, v[68:69]
	s_branch .LBB0_476

; __device__ __forceinline__ void conv8_fill(const Ctx& X, int base, int rank, int nblk, int n) { conv8b_run(X, (base >> 3) + rank, nblk, n); }
; #define SEAM(k) do { if (IN(k) && IN((k) + 1)) xcd_barrier(bar); } while (0)
; __device__ __forceinline__ Cvb conv8b_dec(const Ctx& X, int bit) { Cvb c; int kb, nb;
;     if (bit < I_GU8 / 8) { const int e = bit >> 8, r = bit & 255; kb = r >> 4; nb = r & 15; c.N = 2 * DFF; c.W = XP_w_gu(X) + (size_t)e * D * (2 * DFF); c.WT = XP_WguT(X) + (size_t)e * 16 * PAN_GU + (size_t)kb * PAN_GU; }
;     else { const int b2 = bit - I_GU8 / 8, e = b2 >> 7, r = b2 & 127; kb = r >> 3; nb = r & 7; c.N = D; c.W = XP_w_d(X) + (size_t)e * DFF * D; c.WT = XP_WdT(X) + (size_t)e * 16 * PAN_D + (size_t)kb * PAN_D; }
;     c.W += (size_t)(kb * 128 + 16 * X.wave) * c.N + nb * 256 + 4 * X.lane;
;     c.WT += (size_t)(nb * 256 + 32 * X.wave + (X.lane >> 3)) * 128 + 16 * (X.lane & 7);
;     return c; }
; __device__ __forceinline__ void conv8b_run(const Ctx& X, int first, int step, int count) {
;     if (count <= 0) return;
;     f32x4 v[16];
;     Cvb c = conv8b_dec(X, first), cn = c;
; #pragma unroll
;     for (int i = 0; i < 16; ++i) v[i] = __builtin_nontemporal_load((const f32x4*)(c.W + (size_t)i * c.N));
; __global__ void __launch_bounds__(NTHR, 2) fwd(Args args) {
;     ...
;         if (X.G == 256 && X.bid >= 128) conv8_fill(X, FILL_B4, X.bid - 128, FILL_W4 / NWAVES, FILL_N4); } SEAM(4);
.LBB0_661:
	s_waitcnt lgkmcnt(0)
	s_cmpk_eq_i32 s92, 0x100
	v_readlane_b32 s87, v248, 9
	s_load_dwordx2 s[94:95], s[0:1], 0xa8
	s_cselect_b64 s[2:3], -1, 0
	s_cmpk_gt_i32 s87, 0x7f
	s_cselect_b64 s[4:5], -1, 0
	s_and_b64 s[2:3], s[4:5], s[2:3]
	v_readlane_b32 s96, v248, 7
	v_readlane_b32 s64, v248, 10
	v_readlane_b32 s30, v248, 5
	s_and_b64 vcc, exec, s[2:3]
	v_readlane_b32 s97, v248, 8
	v_readlane_b32 s61, v248, 2
	v_readlane_b32 s62, v248, 3
	v_readlane_b32 s65, v248, 11
	v_readlane_b32 s31, v248, 6
	s_cbranch_vccz .LBB0_671
	s_load_dwordx2 s[4:5], s[0:1], 0x80
	s_add_i32 s2, s87, 0xa00
	s_lshr_b32 s2, s2, 7
	s_mov_b32 s3, 0
	s_bfe_u32 s8, s87, 0x40003
	s_lshl_b64 s[6:7], s[2:3], 24
	s_waitcnt lgkmcnt(0)
	s_mov_b64 s[100:101], s[4:5]
	s_add_u32 s10, s4, s6
	s_addc_u32 s11, s5, s7
	s_add_u32 s18, s90, 0x50000000
	s_addc_u32 s19, s91, 0
	s_lshl_b64 s[4:5], s[2:3], 22
	s_add_u32 s6, s18, s4
	s_addc_u32 s7, s19, s5
	s_lshl_b32 s2, s8, 18
	s_add_u32 s6, s6, s2
	s_mov_b64 s[4:5], s[2:3]
	s_addc_u32 s7, s7, 0
	s_lshl_b32 s2, s87, 8
	s_lshl_b32 s12, s93, 5
	s_and_b32 s13, s2, 0x700
	s_add_i32 s2, s12, s13
	v_lshrrev_b32_e32 v72, 3, v194
	v_or_b32_e32 v66, s2, v72
	s_lshl_b32 s20, s93, 4
	s_lshl_b32 s2, s8, 7
	s_add_i32 s2, s20, s2
	s_lshl_b64 s[8:9], s[2:3], 13
	s_add_u32 s8, s10, s8
	s_addc_u32 s9, s11, s9
	s_lshl_b32 s10, s13, 2
	v_mov_b32_e32 v67, 0
	s_add_u32 s8, s8, s10
	v_lshlrev_b64 v[68:69], 7, v[66:67]
	s_addc_u32 s9, s9, 0
	v_lshlrev_b32_e32 v66, 4, v194
	s_waitcnt vmcnt(2)
	v_lshl_add_u64 v[54:55], s[8:9], 0, v[66:67]
	s_mov_b32 s10, 0x1e000
	v_add_co_u32_e32 v10, vcc, s10, v54
	s_mov_b32 s10, 0x1c000
	s_nop 0
	v_addc_co_u32_e32 v11, vcc, 0, v55, vcc
	v_add_co_u32_e32 v12, vcc, s10, v54
	s_mov_b32 s10, 0x1a000
	s_nop 0
	v_addc_co_u32_e32 v13, vcc, 0, v55, vcc
	v_add_co_u32_e32 v18, vcc, s10, v54
	s_mov_b32 s10, 0x18000
	s_nop 0
	v_addc_co_u32_e32 v19, vcc, 0, v55, vcc
	v_add_co_u32_e32 v20, vcc, s10, v54
	s_mov_b32 s10, 0x16000
	s_nop 0
	v_addc_co_u32_e32 v21, vcc, 0, v55, vcc
	v_add_co_u32_e32 v26, vcc, s10, v54
	s_mov_b32 s10, 0x14000
	s_nop 0
	v_addc_co_u32_e32 v27, vcc, 0, v55, vcc
	v_add_co_u32_e32 v28, vcc, s10, v54
	s_mov_b32 s10, 0x12000
	s_nop 0
	v_addc_co_u32_e32 v29, vcc, 0, v55, vcc
	v_add_co_u32_e32 v34, vcc, s10, v54
	s_mov_b32 s10, 0x10000
	s_nop 0
	v_addc_co_u32_e32 v35, vcc, 0, v55, vcc
	v_add_co_u32_e32 v36, vcc, s10, v54
	s_mov_b32 s10, 0xe000
	s_nop 0
	v_addc_co_u32_e32 v37, vcc, 0, v55, vcc
	s_waitcnt vmcnt(1)
	v_add_co_u32_e32 v42, vcc, s10, v54
	s_mov_b32 s10, 0xc000
	s_nop 0
	v_addc_co_u32_e32 v43, vcc, 0, v55, vcc
	v_add_co_u32_e32 v44, vcc, s10, v54
	s_mov_b32 s10, 0xa000
	s_nop 0
	v_addc_co_u32_e32 v45, vcc, 0, v55, vcc
	s_waitcnt vmcnt(0)
	v_add_co_u32_e32 v50, vcc, s10, v54
	s_mov_b32 s10, 0x8000
	s_nop 0
	v_addc_co_u32_e32 v51, vcc, 0, v55, vcc
	v_add_co_u32_e32 v52, vcc, s10, v54
	s_movk_i32 s10, 0x6000
	s_nop 0
	v_addc_co_u32_e32 v53, vcc, 0, v55, vcc
	v_add_co_u32_e32 v56, vcc, s10, v54
	s_movk_i32 s10, 0x4000
	s_nop 0
	v_addc_co_u32_e32 v57, vcc, 0, v55, vcc
	v_add_co_u32_e32 v62, vcc, s10, v54
	s_movk_i32 s10, 0x2000
	s_nop 0
	v_addc_co_u32_e32 v63, vcc, 0, v55, vcc
	v_add_co_u32_e32 v70, vcc, s10, v54
	global_load_dwordx4 v[2:5], v[10:11], off nt
	global_load_dwordx4 v[6:9], v[12:13], off nt
	v_addc_co_u32_e32 v71, vcc, 0, v55, vcc
	global_load_dwordx4 v[10:13], v[18:19], off nt
	global_load_dwordx4 v[14:17], v[20:21], off nt
	s_nop 0
	global_load_dwordx4 v[18:21], v[26:27], off nt
	global_load_dwordx4 v[22:25], v[28:29], off nt
	s_nop 0
	global_load_dwordx4 v[26:29], v[34:35], off nt
	global_load_dwordx4 v[30:33], v[36:37], off nt
	global_load_dwordx4 v[38:41], v[42:43], off nt
	s_nop 0
	global_load_dwordx4 v[34:37], v[44:45], off nt
	global_load_dwordx4 v[46:49], v[50:51], off nt
	s_nop 0
	global_load_dwordx4 v[42:45], v[52:53], off nt
	global_load_dwordx4 v[58:61], v[56:57], off nt
	s_nop 0
	global_load_dwordx4 v[50:53], v[62:63], off nt
	s_nop 0
	global_load_dwordx4 v[62:65], v[70:71], off nt
	global_load_dwordx4 v[54:57], v66, s[8:9] nt
	v_lshlrev_b32_e32 v66, 4, v0
	v_lshl_add_u64 v[70:71], s[6:7], 0, v[68:69]
	v_and_b32_e32 v68, 0x70, v66
	v_mov_b32_e32 v69, v67
	s_and_b32 s21, s87, 7
	s_and_b32 s22, s87, 15
	v_lshl_add_u64 v[70:71], v[70:71], 0, v[68:69]
	s_mov_b64 s[6:7], s[2:3]
	v_lshlrev_b32_e32 v66, 2, v194
	v_or_b32_e32 v75, s12, v72
	s_add_u32 s23, s90, 0x30000000
	s_movk_i32 s2, 0x90
	v_mul_u32_u24_e32 v74, 0x240, v194
	s_addc_u32 s24, s91, 0
	v_mul_lo_u32 v76, v75, s2
	s_add_i32 s25, s87, 0x2a80
	s_mov_b32 s26, 0xc3e00000
	v_lshlrev_b32_e32 v66, 2, v66
	v_mov_b32_e32 v77, 0x43e00000
	s_mov_b32 s27, 0
	v_mov_b64_e32 v[72:73], v[70:71]
	s_waitcnt vmcnt(0)
	s_branch .LBB0_665

; #define LAS __attribute__((address_space(3)))
; __device__ __forceinline__ Cvb conv8b_dec(const Ctx& X, int bit) { Cvb c; int kb, nb;
;     if (bit < I_GU8 / 8) { const int e = bit >> 8, r = bit & 255; kb = r >> 4; nb = r & 15; c.N = 2 * DFF; c.W = XP_w_gu(X) + (size_t)e * D * (2 * DFF); c.WT = XP_WguT(X) + (size_t)e * 16 * PAN_GU + (size_t)kb * PAN_GU; }
;     else { const int b2 = bit - I_GU8 / 8, e = b2 >> 7, r = b2 & 127; kb = r >> 3; nb = r & 7; c.N = D; c.W = XP_w_d(X) + (size_t)e * DFF * D; c.WT = XP_WdT(X) + (size_t)e * 16 * PAN_D + (size_t)kb * PAN_D; }
;     c.W += (size_t)(kb * 128 + 16 * X.wave) * c.N + nb * 256 + 4 * X.lane;
;     c.WT += (size_t)(nb * 256 + 32 * X.wave + (X.lane >> 3)) * 128 + 16 * (X.lane & 7);
;     return c; }
; __device__ __forceinline__ void conv8b_run(const Ctx& X, int first, int step, int count) {
;     ...
;         LAS uchar* buf = X.lds + (j & 1) * CVT_BUF;
; #pragma unroll
;         for (int q = 0; q < 4; ++q) { u32x4 o;
;             o.x = pk_fp8x4(v[0][q] * W8_SCALE, v[1][q] * W8_SCALE, v[2][q] * W8_SCALE, v[3][q] * W8_SCALE); o.y = pk_fp8x4(v[4][q] * W8_SCALE, v[5][q] * W8_SCALE, v[6][q] * W8_SCALE, v[7][q] * W8_SCALE);
;             o.z = pk_fp8x4(v[8][q] * W8_SCALE, v[9][q] * W8_SCALE, v[10][q] * W8_SCALE, v[11][q] * W8_SCALE); o.w = pk_fp8x4(v[12][q] * W8_SCALE, v[13][q] * W8_SCALE, v[14][q] * W8_SCALE, v[15][q] * W8_SCALE);
;             *(LAS u32x4*)(buf + (4 * X.lane + q) * CVT_STRIDE + 16 * X.wave) = o; }
;         if (j + 1 < count) { cn = conv8b_dec(X, first + (j + 1) * step);
; #pragma unroll
;             for (int i = 0; i < 16; ++i) v[i] = __builtin_nontemporal_load((const f32x4*)(cn.W + (size_t)i * cn.N)); }
.LBB0_665:
	s_waitcnt vmcnt(4)
	v_mul_f32_e32 v78, 0x42800000, v54
	v_mul_f32_e32 v79, 0x42800000, v62
	v_med3_f32 v81, v78, s26, v77
	v_med3_f32 v79, v79, s26, v77
	v_mov_b32_e32 v78, 0
	v_cvt_pk_fp8_f32 v78, v81, v79
	v_mul_f32_e32 v80, 0x42800000, v50
	v_mul_f32_e32 v79, 0x42800000, v58
	v_med3_f32 v80, v80, s26, v77
	v_med3_f32 v79, v79, s26, v77
	v_cvt_pk_fp8_f32 v78, v80, v79 op_sel:[0,0,1]
	v_mul_f32_e32 v79, 0x42800000, v42
	v_mul_f32_e32 v80, 0x42800000, v46
	v_med3_f32 v82, v79, s26, v77
	v_med3_f32 v80, v80, s26, v77
	v_mov_b32_e32 v79, 0
	v_cvt_pk_fp8_f32 v79, v82, v80
	v_mul_f32_e32 v81, 0x42800000, v34
	v_mul_f32_e32 v80, 0x42800000, v38
	v_med3_f32 v81, v81, s26, v77
	v_med3_f32 v80, v80, s26, v77
	v_cvt_pk_fp8_f32 v79, v81, v80 op_sel:[0,0,1]
	v_mul_f32_e32 v80, 0x42800000, v30
	v_mul_f32_e32 v81, 0x42800000, v26
	v_med3_f32 v83, v80, s26, v77
	v_med3_f32 v81, v81, s26, v77
	v_mov_b32_e32 v80, 0
	v_cvt_pk_fp8_f32 v80, v83, v81
	v_mul_f32_e32 v82, 0x42800000, v22
	v_mul_f32_e32 v81, 0x42800000, v18
	v_med3_f32 v82, v82, s26, v77
	v_med3_f32 v81, v81, s26, v77
	v_cvt_pk_fp8_f32 v80, v82, v81 op_sel:[0,0,1]
	v_mul_f32_e32 v81, 0x42800000, v14
	v_mul_f32_e32 v82, 0x42800000, v10
	v_med3_f32 v84, v81, s26, v77
	v_med3_f32 v82, v82, s26, v77
	v_mov_b32_e32 v81, 0
	v_cvt_pk_fp8_f32 v81, v84, v82
	v_mul_f32_e32 v83, 0x42800000, v6
	v_mul_f32_e32 v82, 0x42800000, v2
	s_bitcmp1_b32 s27, 0
	v_med3_f32 v83, v83, s26, v77
	v_med3_f32 v82, v82, s26, v77
	s_cselect_b32 s2, 0x9000, 0
	v_cvt_pk_fp8_f32 v81, v83, v82 op_sel:[0,0,1]
	s_add_i32 s28, s2, 0
	s_add_i32 s2, s20, s28
	v_add_u32_e32 v90, s2, v74
	ds_write_b128 v90, v[78:81]
	v_mul_f32_e32 v78, 0x42800000, v55
	v_mul_f32_e32 v79, 0x42800000, v63
	v_med3_f32 v81, v78, s26, v77
	v_med3_f32 v79, v79, s26, v77
	v_mov_b32_e32 v78, 0
	v_cvt_pk_fp8_f32 v78, v81, v79
	v_mul_f32_e32 v80, 0x42800000, v51
	v_mul_f32_e32 v79, 0x42800000, v59
	v_med3_f32 v80, v80, s26, v77
	v_med3_f32 v79, v79, s26, v77
	v_cvt_pk_fp8_f32 v78, v80, v79 op_sel:[0,0,1]
	v_mul_f32_e32 v79, 0x42800000, v43
	v_mul_f32_e32 v80, 0x42800000, v47
	v_med3_f32 v82, v79, s26, v77
	v_med3_f32 v80, v80, s26, v77
	v_mov_b32_e32 v79, 0
	v_cvt_pk_fp8_f32 v79, v82, v80
	v_mul_f32_e32 v81, 0x42800000, v35
	v_mul_f32_e32 v80, 0x42800000, v39
	v_med3_f32 v81, v81, s26, v77
	v_med3_f32 v80, v80, s26, v77
	v_cvt_pk_fp8_f32 v79, v81, v80 op_sel:[0,0,1]
	v_mul_f32_e32 v80, 0x42800000, v31
	v_mul_f32_e32 v81, 0x42800000, v27
	v_med3_f32 v83, v80, s26, v77
	v_med3_f32 v81, v81, s26, v77
	v_mov_b32_e32 v80, 0
	v_cvt_pk_fp8_f32 v80, v83, v81
	v_mul_f32_e32 v82, 0x42800000, v23
	v_mul_f32_e32 v81, 0x42800000, v19
	v_med3_f32 v82, v82, s26, v77
	v_med3_f32 v81, v81, s26, v77
	v_cvt_pk_fp8_f32 v80, v82, v81 op_sel:[0,0,1]
	v_mul_f32_e32 v81, 0x42800000, v15
	v_mul_f32_e32 v82, 0x42800000, v11
	v_med3_f32 v84, v81, s26, v77
	v_med3_f32 v82, v82, s26, v77
	v_mov_b32_e32 v81, 0
	v_cvt_pk_fp8_f32 v81, v84, v82
	v_mul_f32_e32 v83, 0x42800000, v7
	v_mul_f32_e32 v82, 0x42800000, v3
	v_med3_f32 v83, v83, s26, v77
	v_med3_f32 v82, v82, s26, v77
	v_cvt_pk_fp8_f32 v81, v83, v82 op_sel:[0,0,1]
	v_mul_f32_e32 v82, 0x42800000, v56
	v_mul_f32_e32 v83, 0x42800000, v64
	v_med3_f32 v85, v82, s26, v77
	v_med3_f32 v83, v83, s26, v77
	v_mov_b32_e32 v82, 0
	v_cvt_pk_fp8_f32 v82, v85, v83
	v_mul_f32_e32 v84, 0x42800000, v52
	v_mul_f32_e32 v83, 0x42800000, v60
	v_med3_f32 v84, v84, s26, v77
	v_med3_f32 v83, v83, s26, v77
	v_cvt_pk_fp8_f32 v82, v84, v83 op_sel:[0,0,1]
	v_mul_f32_e32 v83, 0x42800000, v44
	v_mul_f32_e32 v84, 0x42800000, v48
	v_med3_f32 v86, v83, s26, v77
	v_med3_f32 v84, v84, s26, v77
	v_mov_b32_e32 v83, 0
	v_cvt_pk_fp8_f32 v83, v86, v84
	v_mul_f32_e32 v85, 0x42800000, v36
	v_mul_f32_e32 v84, 0x42800000, v40
	v_med3_f32 v85, v85, s26, v77
	v_med3_f32 v84, v84, s26, v77
	v_cvt_pk_fp8_f32 v83, v85, v84 op_sel:[0,0,1]
	v_mul_f32_e32 v84, 0x42800000, v32
	v_mul_f32_e32 v85, 0x42800000, v28
	v_med3_f32 v87, v84, s26, v77
	v_med3_f32 v85, v85, s26, v77
	v_mov_b32_e32 v84, 0
	v_cvt_pk_fp8_f32 v84, v87, v85
	v_mul_f32_e32 v86, 0x42800000, v24
	v_mul_f32_e32 v85, 0x42800000, v20
	v_med3_f32 v86, v86, s26, v77
	v_med3_f32 v85, v85, s26, v77
	v_cvt_pk_fp8_f32 v84, v86, v85 op_sel:[0,0,1]
	v_mul_f32_e32 v85, 0x42800000, v16
	v_mul_f32_e32 v86, 0x42800000, v12
	v_med3_f32 v88, v85, s26, v77
	v_med3_f32 v86, v86, s26, v77
	v_mov_b32_e32 v85, 0
	v_cvt_pk_fp8_f32 v85, v88, v86
	v_mul_f32_e32 v87, 0x42800000, v8
	v_mul_f32_e32 v86, 0x42800000, v4
	v_med3_f32 v87, v87, s26, v77
	v_med3_f32 v86, v86, s26, v77
	v_cvt_pk_fp8_f32 v85, v87, v86 op_sel:[0,0,1]
	v_mul_f32_e32 v86, 0x42800000, v57
	v_mul_f32_e32 v87, 0x42800000, v65
	v_med3_f32 v89, v86, s26, v77
	v_med3_f32 v87, v87, s26, v77
	v_mov_b32_e32 v86, 0
	v_cvt_pk_fp8_f32 v86, v89, v87
	v_mul_f32_e32 v88, 0x42800000, v53
	v_mul_f32_e32 v87, 0x42800000, v61
	v_med3_f32 v88, v88, s26, v77
	v_med3_f32 v87, v87, s26, v77
	v_cvt_pk_fp8_f32 v86, v88, v87 op_sel:[0,0,1]
	v_mul_f32_e32 v87, 0x42800000, v45
	v_mul_f32_e32 v88, 0x42800000, v49
	v_med3_f32 v91, v87, s26, v77
	v_med3_f32 v88, v88, s26, v77
	v_mov_b32_e32 v87, 0
	v_cvt_pk_fp8_f32 v87, v91, v88
	v_mul_f32_e32 v89, 0x42800000, v37
	v_mul_f32_e32 v88, 0x42800000, v41
	v_med3_f32 v89, v89, s26, v77
	v_med3_f32 v88, v88, s26, v77
	v_cvt_pk_fp8_f32 v87, v89, v88 op_sel:[0,0,1]
	v_mul_f32_e32 v88, 0x42800000, v33
	v_mul_f32_e32 v89, 0x42800000, v29
	v_med3_f32 v92, v88, s26, v77
	v_med3_f32 v89, v89, s26, v77
	v_mov_b32_e32 v88, 0
	v_cvt_pk_fp8_f32 v88, v92, v89
	v_mul_f32_e32 v91, 0x42800000, v25
	v_mul_f32_e32 v89, 0x42800000, v21
	v_med3_f32 v91, v91, s26, v77
	v_med3_f32 v89, v89, s26, v77
	v_cvt_pk_fp8_f32 v88, v91, v89 op_sel:[0,0,1]
	v_mul_f32_e32 v89, 0x42800000, v17
	v_mul_f32_e32 v91, 0x42800000, v13
	v_med3_f32 v93, v89, s26, v77
	v_med3_f32 v91, v91, s26, v77
	v_mov_b32_e32 v89, 0
	v_cvt_pk_fp8_f32 v89, v93, v91
	v_mul_f32_e32 v92, 0x42800000, v9
	v_mul_f32_e32 v91, 0x42800000, v5
	v_med3_f32 v92, v92, s26, v77
	v_med3_f32 v91, v91, s26, v77
	v_cvt_pk_fp8_f32 v89, v92, v91 op_sel:[0,0,1]
	s_cmp_gt_u32 s27, 9
	ds_write_b128 v90, v[78:81] offset:144
	ds_write_b128 v90, v[82:85] offset:288
	ds_write_b128 v90, v[86:89] offset:432
	s_cbranch_scc1 .LBB0_664
	s_cmpk_gt_i32 s25, 0x1fff
	s_mov_b64 s[14:15], -1
	s_cbranch_scc0 .LBB0_668
	s_mov_b64 s[8:9], s[100:101]
	s_add_i32 s2, s25, 0xffffe000
	s_lshr_b32 s2, s2, 7
	s_lshl_b64 s[10:11], s[2:3], 24
	s_mov_b64 s[14:15], 0
	s_waitcnt lgkmcnt(0)
	s_add_u32 s8, s8, s10
	s_addc_u32 s9, s9, s11
	s_lshl_b64 s[10:11], s[2:3], 22
	s_add_u32 s10, s18, s10
	s_addc_u32 s11, s19, s11
